# P13/P15 streaming accesses (ids, h2, PA, X) tagged nt to keep the gathered table slice in L2
# baseline (speedup 1.0000x reference)
; #define LDS_WAIT() asm volatile("s_waitcnt lgkmcnt(0)" ::: "memory")
; __device__ __forceinline__ void phase_peer_a(const Frame& F, const Args& a, const int emask, float* PA) {
;     ...
;         u32x4 hq0, hn0 = {0, 0, 0, 0}; int pn0 = 0, pn1 = 0;
;         { hq0 = *(const u32x4*)(H2Q + (size_t)tok * D + sl * 256 + li * 16);
;           lpe[lane] = PE[(size_t)tok * 128 + lane] & emask; lpe[64 + lane] = PE[(size_t)tok * 128 + 64 + lane] & emask; lpe[128 + lane] = 0; lpe[192 + lane] = 0;
;           if (tok + step < T) { pn0 = PE[(size_t)(tok + step) * 128 + lane]; pn1 = PE[(size_t)(tok + step) * 128 + 64 + lane]; } }
;         LDS_WAIT();
.LBB0_1452:
	s_and_b64 vcc, exec, s[14:15]
	s_cbranch_vccnz .LBB0_1451
	s_or_b32 s26, s5, s35
	s_lshl_b32 s0, s26, 8
	global_load_dword v3, v[148:149], off nt
	global_load_dword v6, v[148:149], off offset:256 nt
	v_lshl_add_u64 v[4:5], v[146:147], 0, s[0:1]
	global_load_dwordx4 v[10:13], v[4:5], off nt
	v_mov_b32_e32 v143, 0
	s_and_b64 vcc, exec, s[16:17]
	v_mov_b32_e32 v145, 0
	ds_write2st64_b32 v1, v143, v143 offset0:2 offset1:3
	s_waitcnt vmcnt(2)
	v_and_b32_e32 v3, 0x3fff, v3
	s_waitcnt vmcnt(1)
	v_and_b32_e32 v4, 0x3fff, v6
	ds_write2st64_b32 v1, v3, v4 offset1:1
	s_cbranch_vccnz .LBB0_1455
	global_load_dword v145, v[150:151], off nt
	global_load_dword v143, v[150:151], off offset:256 nt

; #define LDS_WAIT() asm volatile("s_waitcnt lgkmcnt(0)" ::: "memory")
; #define PA_LOADS(dst, buf, half) do { _Pragma("unroll") for (int j = 0; j < 16; ++j) { const unsigned e = (unsigned)lpe[(buf) * 128 + 4 * ((half) * 16 + j) + rg]; dst[j] = *(const u32x4*)(Us + (size_t)(e * 256u + lo16)); } } while (0)
; __device__ __forceinline__ void phase_peer_a(const Frame& F, const Args& a, const int emask, float* PA) {
;     ...
;             PA_LOADS(wB, cur, 1);
;             int v[32];
; #pragma unroll
;             for (int j = 0; j < 16; ++j) v[j] = idot16(wA[j], hq0);
;             LDS_WAIT();
;             PA_LOADS(wA, cur ^ 1, 0);
; #pragma unroll
;             for (int j = 0; j < 16; ++j) v[16 + j] = idot16(wB[j], hq0);
.LBB0_1456:
	v_lshl_add_u32 v3, s0, 9, v162
	ds_read2_b32 v[4:5], v3 offset0:64 offset1:68
	ds_read2_b32 v[78:79], v3 offset0:72 offset1:76
	v_mov_b32_e32 v177, 0
	s_waitcnt vmcnt(2)
	v_dot4c_i32_i8_e32 v177, v6, v10
	v_dot4c_i32_i8_e32 v177, v7, v11
	s_waitcnt lgkmcnt(1)
	v_lshl_or_b32 v4, v4, 8, v144
	v_lshl_or_b32 v5, v5, 8, v144
	global_load_dwordx4 v[138:141], v4, s[26:27]
	global_load_dwordx4 v[134:137], v5, s[26:27]
	ds_read2_b32 v[4:5], v3 offset0:80 offset1:84
	s_waitcnt lgkmcnt(1)
	v_lshl_or_b32 v78, v78, 8, v144
	v_lshl_or_b32 v79, v79, 8, v144
	global_load_dwordx4 v[130:133], v78, s[26:27]
	global_load_dwordx4 v[122:125], v79, s[26:27]
	ds_read2_b32 v[78:79], v3 offset0:88 offset1:92
	s_waitcnt lgkmcnt(1)
	v_lshl_or_b32 v4, v4, 8, v144
	v_lshl_or_b32 v5, v5, 8, v144
	global_load_dwordx4 v[126:129], v4, s[26:27]
	global_load_dwordx4 v[118:121], v5, s[26:27]
	ds_read2_b32 v[4:5], v3 offset0:96 offset1:100
	s_waitcnt lgkmcnt(1)
	v_lshl_or_b32 v78, v78, 8, v144
	v_lshl_or_b32 v79, v79, 8, v144
	global_load_dwordx4 v[114:117], v78, s[26:27]
	global_load_dwordx4 v[106:109], v79, s[26:27]
	ds_read2_b32 v[78:79], v3 offset0:104 offset1:108
	s_waitcnt lgkmcnt(1)
	v_lshl_or_b32 v4, v4, 8, v144
	v_lshl_or_b32 v5, v5, 8, v144
	global_load_dwordx4 v[110:113], v4, s[26:27]
	global_load_dwordx4 v[102:105], v5, s[26:27]
	ds_read2_b32 v[4:5], v3 offset0:112 offset1:116
	s_waitcnt lgkmcnt(1)
	v_lshl_or_b32 v78, v78, 8, v144
	v_lshl_or_b32 v79, v79, 8, v144
	global_load_dwordx4 v[98:101], v78, s[26:27]
	global_load_dwordx4 v[90:93], v79, s[26:27]
	ds_read2_b32 v[78:79], v3 offset0:120 offset1:124
	s_waitcnt lgkmcnt(1)
	v_lshl_or_b32 v3, v4, 8, v144
	v_lshl_or_b32 v4, v5, 8, v144
	global_load_dwordx4 v[94:97], v3, s[26:27]
	global_load_dwordx4 v[86:89], v4, s[26:27]
	v_dot4c_i32_i8_e32 v177, v8, v12
	s_waitcnt lgkmcnt(0)
	v_lshl_or_b32 v3, v78, 8, v144
	v_lshl_or_b32 v4, v79, 8, v144
	global_load_dwordx4 v[82:85], v3, s[26:27]
	global_load_dwordx4 v[78:81], v4, s[26:27]
	s_waitcnt lgkmcnt(0)
	v_lshl_add_u32 v4, s36, 2, v162
	v_lshl_add_u32 v8, s36, 2, v162
	ds_read_b32 v6, v4
	v_dot4c_i32_i8_e32 v177, v9, v13
	ds_read_b32 v9, v8 offset:240
	ds_read2_b32 v[4:5], v8 offset0:4 offset1:8
	v_mov_b32_e32 v3, 0
	v_mov_b32_e32 v163, 0
	s_waitcnt vmcnt(16)
	v_dot4c_i32_i8_e32 v3, v74, v10
	v_dot4c_i32_i8_e32 v163, v70, v10
	v_dot4c_i32_i8_e32 v3, v75, v11
	v_dot4c_i32_i8_e32 v163, v71, v11
	v_mov_b32_e32 v176, 0
	v_dot4c_i32_i8_e32 v3, v76, v12
	v_dot4c_i32_i8_e32 v163, v72, v12
	v_dot4c_i32_i8_e32 v176, v14, v10
	s_waitcnt lgkmcnt(2)
	v_lshl_or_b32 v14, v6, 8, v144
	ds_read2_b32 v[6:7], v8 offset0:12 offset1:16
	s_waitcnt lgkmcnt(1)
	v_lshl_or_b32 v4, v4, 8, v144
	v_dot4c_i32_i8_e32 v3, v77, v13
	v_dot4c_i32_i8_e32 v163, v73, v13
	global_load_dwordx4 v[74:77], v14, s[26:27]
	global_load_dwordx4 v[70:73], v4, s[26:27]
	v_lshl_or_b32 v14, v5, 8, v144
	ds_read2_b32 v[4:5], v8 offset0:20 offset1:24
	v_mov_b32_e32 v164, 0
	v_mov_b32_e32 v165, 0
	v_dot4c_i32_i8_e32 v164, v66, v10
	v_dot4c_i32_i8_e32 v165, v62, v10
	v_mov_b32_e32 v166, 0
	v_mov_b32_e32 v167, 0
	v_dot4c_i32_i8_e32 v164, v67, v11
	v_dot4c_i32_i8_e32 v165, v63, v11
	v_dot4c_i32_i8_e32 v166, v58, v10
	v_dot4c_i32_i8_e32 v167, v54, v10
	v_dot4c_i32_i8_e32 v164, v68, v12
	v_dot4c_i32_i8_e32 v165, v64, v12
	v_dot4c_i32_i8_e32 v166, v59, v11
	v_dot4c_i32_i8_e32 v167, v55, v11
	s_waitcnt lgkmcnt(1)
	v_lshl_or_b32 v6, v6, 8, v144
	v_dot4c_i32_i8_e32 v164, v69, v13
	v_dot4c_i32_i8_e32 v165, v65, v13
	v_dot4c_i32_i8_e32 v166, v60, v12
	v_dot4c_i32_i8_e32 v167, v56, v12
	global_load_dwordx4 v[66:69], v14, s[26:27]
	global_load_dwordx4 v[62:65], v6, s[26:27]
	v_lshl_or_b32 v14, v7, 8, v144
	s_waitcnt lgkmcnt(0)
	v_lshl_or_b32 v4, v4, 8, v144
	ds_read2_b32 v[6:7], v8 offset0:28 offset1:32
	v_dot4c_i32_i8_e32 v166, v61, v13
	v_dot4c_i32_i8_e32 v167, v57, v13
	global_load_dwordx4 v[58:61], v14, s[26:27]
	global_load_dwordx4 v[54:57], v4, s[26:27]
	v_lshl_or_b32 v14, v5, 8, v144
	ds_read2_b32 v[4:5], v8 offset0:36 offset1:40
	v_mov_b32_e32 v168, 0
	v_mov_b32_e32 v169, 0
	v_dot4c_i32_i8_e32 v168, v50, v10
	v_dot4c_i32_i8_e32 v169, v46, v10
	v_mov_b32_e32 v170, 0
	v_mov_b32_e32 v171, 0
	v_dot4c_i32_i8_e32 v168, v51, v11
	v_dot4c_i32_i8_e32 v169, v47, v11
	v_dot4c_i32_i8_e32 v170, v42, v10
	v_dot4c_i32_i8_e32 v171, v38, v10
	v_dot4c_i32_i8_e32 v168, v52, v12
	v_dot4c_i32_i8_e32 v169, v48, v12
	v_dot4c_i32_i8_e32 v170, v43, v11
	v_dot4c_i32_i8_e32 v171, v39, v11
	s_waitcnt lgkmcnt(1)
	v_lshl_or_b32 v6, v6, 8, v144
	v_dot4c_i32_i8_e32 v168, v53, v13
	v_dot4c_i32_i8_e32 v169, v49, v13
	v_dot4c_i32_i8_e32 v170, v44, v12
	v_dot4c_i32_i8_e32 v171, v40, v12
	global_load_dwordx4 v[50:53], v14, s[26:27]
	global_load_dwordx4 v[46:49], v6, s[26:27]
	v_lshl_or_b32 v14, v7, 8, v144
	s_waitcnt lgkmcnt(0)
	v_lshl_or_b32 v4, v4, 8, v144
	ds_read2_b32 v[6:7], v8 offset0:44 offset1:48
	v_dot4c_i32_i8_e32 v170, v45, v13
	v_dot4c_i32_i8_e32 v171, v41, v13
	global_load_dwordx4 v[42:45], v14, s[26:27]
	global_load_dwordx4 v[38:41], v4, s[26:27]
	v_lshl_or_b32 v14, v5, 8, v144
	ds_read2_b32 v[4:5], v8 offset0:52 offset1:56
	v_mov_b32_e32 v172, 0
	v_mov_b32_e32 v173, 0
	v_dot4c_i32_i8_e32 v172, v34, v10
	v_dot4c_i32_i8_e32 v173, v30, v10
	v_mov_b32_e32 v174, 0
	v_mov_b32_e32 v175, 0
	v_dot4c_i32_i8_e32 v172, v35, v11
	v_dot4c_i32_i8_e32 v173, v31, v11
	v_dot4c_i32_i8_e32 v174, v26, v10
	v_dot4c_i32_i8_e32 v175, v22, v10
	v_dot4c_i32_i8_e32 v172, v36, v12
	v_dot4c_i32_i8_e32 v173, v32, v12
	v_dot4c_i32_i8_e32 v174, v27, v11
	v_dot4c_i32_i8_e32 v175, v23, v11
	s_waitcnt lgkmcnt(1)
; #define LDS_WAIT() asm volatile("s_waitcnt lgkmcnt(0)" ::: "memory")
; #define PA_LOADS(dst, buf, half) do { _Pragma("unroll") for (int j = 0; j < 16; ++j) { const unsigned e = (unsigned)lpe[(buf) * 128 + 4 * ((half) * 16 + j) + rg]; dst[j] = *(const u32x4*)(Us + (size_t)(e * 256u + lo16)); } } while (0)
; __device__ __forceinline__ void phase_peer_a(const Frame& F, const Args& a, const int emask, float* PA) {
;     ...
;             PA_LOADS(wB, cur, 1);
;             int v[32];
; #pragma unroll
;             for (int j = 0; j < 16; ++j) v[j] = idot16(wA[j], hq0);
;             LDS_WAIT();
;             PA_LOADS(wA, cur ^ 1, 0);
; #pragma unroll
;             for (int j = 0; j < 16; ++j) v[16 + j] = idot16(wB[j], hq0);
	v_lshl_or_b32 v6, v6, 8, v144
	v_dot4c_i32_i8_e32 v172, v37, v13
	v_dot4c_i32_i8_e32 v173, v33, v13
	v_dot4c_i32_i8_e32 v174, v28, v12
	v_dot4c_i32_i8_e32 v175, v24, v12
	v_dot4c_i32_i8_e32 v176, v15, v11
	global_load_dwordx4 v[34:37], v14, s[26:27]
	global_load_dwordx4 v[30:33], v6, s[26:27]
	v_lshl_or_b32 v6, v7, 8, v144
	s_waitcnt lgkmcnt(0)
	v_lshl_or_b32 v4, v4, 8, v144
	v_dot4c_i32_i8_e32 v174, v29, v13
	v_dot4c_i32_i8_e32 v175, v25, v13
	v_dot4c_i32_i8_e32 v176, v16, v12
	global_load_dwordx4 v[26:29], v6, s[26:27]
	global_load_dwordx4 v[22:25], v4, s[26:27]
	v_lshl_or_b32 v4, v5, 8, v144
	v_dot4c_i32_i8_e32 v176, v17, v13
	v_lshl_or_b32 v5, v9, 8, v144
	global_load_dwordx4 v[14:17], v4, s[26:27]
	global_load_dwordx4 v[6:9], v5, s[26:27]
	v_mov_b32_e32 v5, 0
	s_waitcnt vmcnt(30)
	v_dot4c_i32_i8_e32 v5, v134, v10
	v_mov_b32_e32 v134, 0
	s_waitcnt vmcnt(29)
	v_dot4c_i32_i8_e32 v134, v130, v10
	v_mov_b32_e32 v130, 0
	s_waitcnt vmcnt(28)
	v_dot4c_i32_i8_e32 v130, v122, v10
	v_dot4c_i32_i8_e32 v130, v123, v11
	v_mov_b32_e32 v123, 0
	s_waitcnt vmcnt(26)
	v_dot4c_i32_i8_e32 v123, v118, v10
	v_mov_b32_e32 v118, 0
	s_waitcnt vmcnt(25)
	v_dot4c_i32_i8_e32 v118, v114, v10
	v_mov_b32_e32 v114, 0
	s_waitcnt vmcnt(24)
	v_dot4c_i32_i8_e32 v114, v106, v10
	v_dot4c_i32_i8_e32 v114, v107, v11
	v_mov_b32_e32 v107, 0
	s_waitcnt vmcnt(22)
	v_dot4c_i32_i8_e32 v107, v102, v10
	v_mov_b32_e32 v102, 0
	v_mov_b32_e32 v4, 0
	s_waitcnt vmcnt(21)
	v_dot4c_i32_i8_e32 v102, v98, v10
	v_mov_b32_e32 v98, 0
	v_dot4c_i32_i8_e32 v4, v138, v10
	s_waitcnt vmcnt(20)
	v_dot4c_i32_i8_e32 v98, v90, v10
	v_dot4c_i32_i8_e32 v4, v139, v11
	v_dot4c_i32_i8_e32 v5, v135, v11
	v_dot4c_i32_i8_e32 v98, v91, v11
	v_mov_b32_e32 v91, 0
	v_dot4c_i32_i8_e32 v4, v140, v12
	v_dot4c_i32_i8_e32 v5, v136, v12
	v_dot4c_i32_i8_e32 v134, v131, v11
	v_mov_b32_e32 v122, 0
	s_waitcnt vmcnt(18)
	v_dot4c_i32_i8_e32 v91, v86, v10
	v_mov_b32_e32 v86, 0
	v_dot4c_i32_i8_e32 v4, v141, v13
	v_dot4c_i32_i8_e32 v5, v137, v13
	v_dot4c_i32_i8_e32 v134, v132, v12
	v_dot4c_i32_i8_e32 v122, v126, v10
	v_mov_b32_e32 v106, 0
	v_mov_b32_e32 v90, 0
	s_waitcnt vmcnt(17)
	v_dot4c_i32_i8_e32 v86, v82, v10
	v_mov_b32_e32 v82, 0
	v_dot4c_i32_i8_e32 v134, v133, v13
	v_dot4c_i32_i8_e32 v130, v124, v12
	v_dot4c_i32_i8_e32 v122, v127, v11
	v_dot4c_i32_i8_e32 v106, v110, v10
	v_dot4c_i32_i8_e32 v90, v94, v10
	s_waitcnt vmcnt(16)
; #define PA_STEP(N, B, CTRL) _Pragma("unroll") for (int i = 0; i < N; ++i) { const int snd = B ? v[i] : v[N + i], kp = B ? v[N + i] : v[i]; v[i] = kp + __builtin_amdgcn_update_dpp(0, snd, CTRL, 0xf, 0xf, false); }
; __device__ __forceinline__ void phase_peer_a(const Frame& F, const Args& a, const int emask, float* PA) {
;     ...
;             for (int j = 0; j < 16; ++j) v[16 + j] = idot16(wB[j], hq0);
;     ...
;             PA_STEP(16, b3, 0x128) PA_STEP(8, b2, 0x141) PA_STEP(4, b1, 0x4E) PA_STEP(2, b0, 0xB1)
;     ...
;             float* pa = PA + ((size_t)sl * T + tok) * 128 + rg;
;             pa[4 * (2 * li)] = (float)v[0]; pa[4 * (2 * li + 1)] = (float)v[1];
;             hq0 = hn0; cur ^= 1;
	v_dot4c_i32_i8_e32 v82, v78, v10
	v_cndmask_b32_e64 v10, v3, v4, s[6:7]
	v_cndmask_b32_e64 v3, v4, v3, s[6:7]
	v_cndmask_b32_e64 v4, v163, v5, s[6:7]
	v_cndmask_b32_e64 v5, v5, v163, s[6:7]
	v_dot4c_i32_i8_e32 v130, v125, v13
	v_dot4c_i32_i8_e32 v122, v128, v12
	v_dot4c_i32_i8_e32 v123, v119, v11
	v_add_u32_dpp v3, v10, v3 row_ror:8 row_mask:0xf bank_mask:0xf bound_ctrl:1
	v_add_u32_dpp v4, v4, v5 row_ror:8 row_mask:0xf bank_mask:0xf bound_ctrl:1
	v_cndmask_b32_e64 v5, v164, v134, s[6:7]
	v_cndmask_b32_e64 v10, v134, v164, s[6:7]
	v_dot4c_i32_i8_e32 v122, v129, v13
	v_dot4c_i32_i8_e32 v123, v120, v12
	v_dot4c_i32_i8_e32 v118, v115, v11
	v_dot4c_i32_i8_e32 v106, v111, v11
	v_dot4c_i32_i8_e32 v107, v103, v11
	v_dot4c_i32_i8_e32 v102, v99, v11
	v_dot4c_i32_i8_e32 v90, v95, v11
	v_dot4c_i32_i8_e32 v91, v87, v11
	v_dot4c_i32_i8_e32 v86, v83, v11
	v_dot4c_i32_i8_e32 v82, v79, v11
	v_add_u32_dpp v5, v5, v10 row_ror:8 row_mask:0xf bank_mask:0xf bound_ctrl:1
	v_cndmask_b32_e64 v10, v165, v130, s[6:7]
	v_cndmask_b32_e64 v11, v130, v165, s[6:7]
	v_dot4c_i32_i8_e32 v123, v121, v13
	v_dot4c_i32_i8_e32 v118, v116, v12
	v_dot4c_i32_i8_e32 v114, v108, v12
	v_dot4c_i32_i8_e32 v106, v112, v12
	v_dot4c_i32_i8_e32 v107, v104, v12
	v_dot4c_i32_i8_e32 v102, v100, v12
	v_dot4c_i32_i8_e32 v98, v92, v12
	v_dot4c_i32_i8_e32 v90, v96, v12
	v_dot4c_i32_i8_e32 v91, v88, v12
	v_dot4c_i32_i8_e32 v86, v84, v12
	v_dot4c_i32_i8_e32 v82, v80, v12
	v_add_u32_dpp v10, v10, v11 row_ror:8 row_mask:0xf bank_mask:0xf bound_ctrl:1
	v_cndmask_b32_e64 v11, v166, v122, s[6:7]
	v_cndmask_b32_e64 v12, v122, v166, s[6:7]
	v_dot4c_i32_i8_e32 v118, v117, v13
	v_dot4c_i32_i8_e32 v114, v109, v13
	v_dot4c_i32_i8_e32 v106, v113, v13
	v_dot4c_i32_i8_e32 v107, v105, v13
	v_dot4c_i32_i8_e32 v102, v101, v13
	v_dot4c_i32_i8_e32 v98, v93, v13
	v_dot4c_i32_i8_e32 v90, v97, v13
	v_dot4c_i32_i8_e32 v91, v89, v13
	v_dot4c_i32_i8_e32 v86, v85, v13
	v_dot4c_i32_i8_e32 v82, v81, v13
	v_add_u32_dpp v11, v11, v12 row_ror:8 row_mask:0xf bank_mask:0xf bound_ctrl:1
	v_cndmask_b32_e64 v12, v167, v123, s[6:7]
	v_cndmask_b32_e64 v13, v123, v167, s[6:7]
	v_cndmask_b32_e64 v78, v118, v168, s[6:7]
	v_cndmask_b32_e64 v79, v114, v169, s[6:7]
	v_add_u32_dpp v12, v12, v13 row_ror:8 row_mask:0xf bank_mask:0xf bound_ctrl:1
	v_cndmask_b32_e64 v13, v168, v118, s[6:7]
	v_cndmask_b32_e64 v80, v106, v170, s[6:7]
	v_cndmask_b32_e64 v81, v107, v171, s[6:7]
	v_add_u32_dpp v13, v13, v78 row_ror:8 row_mask:0xf bank_mask:0xf bound_ctrl:1
	v_cndmask_b32_e64 v78, v169, v114, s[6:7]
	v_cndmask_b32_e64 v83, v102, v172, s[6:7]
	v_cndmask_b32_e64 v84, v98, v173, s[6:7]
	v_add_u32_dpp v78, v78, v79 row_ror:8 row_mask:0xf bank_mask:0xf bound_ctrl:1
	v_cndmask_b32_e64 v79, v170, v106, s[6:7]
	v_cndmask_b32_e64 v85, v90, v174, s[6:7]
	v_cndmask_b32_e64 v87, v91, v175, s[6:7]
	v_add_u32_dpp v79, v79, v80 row_ror:8 row_mask:0xf bank_mask:0xf bound_ctrl:1
	v_cndmask_b32_e64 v80, v171, v107, s[6:7]
	s_xor_b32 s0, s0, 1
	v_lshl_add_u64 v[160:161], v[160:161], 0, s[22:23]
	v_add_u32_dpp v80, v80, v81 row_ror:8 row_mask:0xf bank_mask:0xf bound_ctrl:1
	v_cndmask_b32_e64 v81, v172, v102, s[6:7]
	s_andn2_b64 vcc, exec, s[28:29]
	s_mov_b32 s37, s5
	v_add_u32_dpp v81, v81, v83 row_ror:8 row_mask:0xf bank_mask:0xf bound_ctrl:1
	v_cndmask_b32_e64 v83, v173, v98, s[6:7]
	s_nop 1
	v_add_u32_dpp v83, v83, v84 row_ror:8 row_mask:0xf bank_mask:0xf bound_ctrl:1
	v_cndmask_b32_e64 v84, v174, v90, s[6:7]
	s_nop 1
	v_add_u32_dpp v84, v84, v85 row_ror:8 row_mask:0xf bank_mask:0xf bound_ctrl:1
	v_cndmask_b32_e64 v85, v175, v91, s[6:7]
	s_nop 1
	v_add_u32_dpp v85, v85, v87 row_ror:8 row_mask:0xf bank_mask:0xf bound_ctrl:1
	v_cndmask_b32_e64 v87, v176, v86, s[6:7]
	v_cndmask_b32_e64 v86, v86, v176, s[6:7]
	s_nop 1
	v_add_u32_dpp v86, v87, v86 row_ror:8 row_mask:0xf bank_mask:0xf bound_ctrl:1
	v_cndmask_b32_e64 v87, v177, v82, s[6:7]
	v_cndmask_b32_e64 v82, v82, v177, s[6:7]
	s_nop 1
	v_add_u32_dpp v82, v87, v82 row_ror:8 row_mask:0xf bank_mask:0xf bound_ctrl:1
	v_cndmask_b32_e64 v87, v3, v79, s[8:9]
	v_cndmask_b32_e64 v3, v79, v3, s[8:9]
	v_cndmask_b32_e64 v79, v4, v80, s[8:9]
	v_cndmask_b32_e64 v4, v80, v4, s[8:9]
	v_add_u32_dpp v3, v87, v3 row_half_mirror row_mask:0xf bank_mask:0xf bound_ctrl:1
	s_nop 0
	v_add_u32_dpp v4, v79, v4 row_half_mirror row_mask:0xf bank_mask:0xf bound_ctrl:1
	v_cndmask_b32_e64 v79, v5, v81, s[8:9]
	v_cndmask_b32_e64 v5, v81, v5, s[8:9]
	s_nop 1
	v_add_u32_dpp v5, v79, v5 row_half_mirror row_mask:0xf bank_mask:0xf bound_ctrl:1
	v_cndmask_b32_e64 v79, v10, v83, s[8:9]
	v_cndmask_b32_e64 v10, v83, v10, s[8:9]
	s_nop 1
	v_add_u32_dpp v10, v79, v10 row_half_mirror row_mask:0xf bank_mask:0xf bound_ctrl:1
	v_cndmask_b32_e64 v79, v11, v84, s[8:9]
	v_cndmask_b32_e64 v11, v84, v11, s[8:9]
	s_nop 1
	v_add_u32_dpp v11, v79, v11 row_half_mirror row_mask:0xf bank_mask:0xf bound_ctrl:1
	v_cndmask_b32_e64 v79, v12, v85, s[8:9]
	v_cndmask_b32_e64 v12, v85, v12, s[8:9]
	s_nop 1
	v_add_u32_dpp v12, v79, v12 row_half_mirror row_mask:0xf bank_mask:0xf bound_ctrl:1
	v_cndmask_b32_e64 v79, v13, v86, s[8:9]
	v_cndmask_b32_e64 v13, v86, v13, s[8:9]
	s_nop 1
	v_add_u32_dpp v13, v79, v13 row_half_mirror row_mask:0xf bank_mask:0xf bound_ctrl:1
	v_cndmask_b32_e64 v79, v78, v82, s[8:9]
	v_cndmask_b32_e64 v78, v82, v78, s[8:9]
	s_nop 1
	v_add_u32_dpp v78, v79, v78 row_half_mirror row_mask:0xf bank_mask:0xf bound_ctrl:1
	v_cndmask_b32_e64 v79, v3, v11, s[10:11]
	v_cndmask_b32_e64 v3, v11, v3, s[10:11]
	v_cndmask_b32_e64 v11, v4, v12, s[10:11]
	v_cndmask_b32_e64 v4, v12, v4, s[10:11]
	v_add_u32_dpp v3, v79, v3 quad_perm:[2,3,0,1] row_mask:0xf bank_mask:0xf bound_ctrl:1
	s_nop 0
	v_add_u32_dpp v4, v11, v4 quad_perm:[2,3,0,1] row_mask:0xf bank_mask:0xf bound_ctrl:1
	v_cndmask_b32_e64 v11, v5, v13, s[10:11]
	v_cndmask_b32_e64 v5, v13, v5, s[10:11]
	s_nop 1
	v_add_u32_dpp v5, v11, v5 quad_perm:[2,3,0,1] row_mask:0xf bank_mask:0xf bound_ctrl:1
	v_cndmask_b32_e64 v11, v10, v78, s[10:11]
	v_cndmask_b32_e64 v10, v78, v10, s[10:11]
	s_nop 1
	v_add_u32_dpp v10, v11, v10 quad_perm:[2,3,0,1] row_mask:0xf bank_mask:0xf bound_ctrl:1
	v_cndmask_b32_e64 v11, v3, v5, s[12:13]
	v_cndmask_b32_e64 v3, v5, v3, s[12:13]
	v_cndmask_b32_e64 v5, v4, v10, s[12:13]
	v_cndmask_b32_e64 v4, v10, v4, s[12:13]
	v_add_u32_dpp v3, v11, v3 quad_perm:[1,0,3,2] row_mask:0xf bank_mask:0xf bound_ctrl:1
	v_cvt_f32_i32_e32 v3, v3
	v_add_u32_dpp v4, v5, v4 quad_perm:[1,0,3,2] row_mask:0xf bank_mask:0xf bound_ctrl:1
	v_cvt_f32_i32_e32 v4, v4
	v_mov_b64_e32 v[10:11], v[18:19]
	global_store_dword v[158:159], v3, off nt
	global_store_dword v[158:159], v4, off offset:16 nt
	v_lshl_add_u64 v[158:159], v[158:159], 0, s[20:21]
	v_mov_b64_e32 v[12:13], v[20:21]
	s_cbranch_vccz .LBB0_1450

; __device__ __forceinline__ void phase_peer_a(const Frame& F, const Args& a, const int emask, float* PA) {
;     ...
;             const int tn = tok + step; const bool has_next = tn < T;
;             if (has_next) { lpe[(cur ^ 1) * 128 + lane] = pn0 & emask; lpe[(cur ^ 1) * 128 + 64 + lane] = pn1 & emask;
;                 hn0 = *(const u32x4*)(H2Q + (size_t)tn * D + sl * 256 + li * 16);
;                 if (tn + step < T) { pn0 = PE[(size_t)(tn + step) * 128 + lane]; pn1 = PE[(size_t)(tn + step) * 128 + 64 + lane]; } }
.LBB0_1459:
	s_andn2_b64 vcc, exec, s[30:31]
	s_cbranch_vccnz .LBB0_1456
	global_load_dwordx4 v[18:21], v[160:161], off nt
	s_lshl_b32 s30, s0, 7
	s_xor_b32 s36, s30, 0x80
	s_add_i32 s30, s3, s37
	s_waitcnt vmcnt(18)
	v_and_b32_e32 v3, 0x3fff, v145
	v_lshl_add_u32 v4, s36, 2, v1
	s_waitcnt vmcnt(17)
	v_and_b32_e32 v5, 0x3fff, v143
	s_cmpk_gt_i32 s30, 0x1fff
	ds_write2st64_b32 v4, v3, v5 offset1:1
	s_cbranch_scc1 .LBB0_1456
	s_ashr_i32 s31, s30, 31
	s_lshl_b64 s[30:31], s[30:31], 9
	v_lshl_add_u64 v[4:5], v[152:153], 0, s[30:31]
	global_load_dword v145, v[4:5], off nt
	global_load_dword v143, v[4:5], off offset:256 nt
	s_branch .LBB0_1456

; #define LDS_WAIT() asm volatile("s_waitcnt lgkmcnt(0)" ::: "memory")
; __device__ __forceinline__ void phase_peer_v(const Frame& F, const Args& a, const bool dry) {
;     ...
;         if (tok < T) { pn0 = PE[(size_t)tok * 128 + lane]; pn1 = PE[(size_t)tok * 128 + 64 + lane]; cn = CQ[(size_t)tok * 32 + (lane & 31)]; }
;         for (; tok < T; tok += nrank * 8) {
;             lpe[lane] = pn0; lpe[64 + lane] = pn1; if (lane < 32) lcq[lane] = cn;
;             LDS_WAIT();
;             { const int tn = tok + nrank * 8; if (tn < T) { pn0 = PE[(size_t)tn * 128 + lane]; pn1 = PE[(size_t)tn * 128 + 64 + lane]; cn = CQ[(size_t)tn * 32 + (lane & 31)]; } }
;             u32x2* xp = (u32x2*)(X + (size_t)tok * D + sl * 256 + li * 16 + rg * 4);
;             const u32x2 xb = *xp; const f32x4 xq = {bflo(xb.x), bfhi(xb.x), bflo(xb.y), bfhi(xb.y)};
;             const float csc = CSC[tok];
;             i32x4 acc = {0, 0, 0, 0};
; #pragma unroll
;             for (int q8 = 0; q8 < 32 / PS_B; ++q8) { u32x4 w[PS_B]; unsigned cd[PS_B];
; #pragma unroll
;                 for (int j = 0; j < PS_B; ++j) { const int q = q8 * PS_B + j; const int e = lpe[4 * q + rg]; cd[j] = lcq[q]; w[j] = *(const u32x4*)(Vs + (size_t)e * 256); }
.LBB0_1583:
	s_and_b64 vcc, exec, s[16:17]
	s_cbranch_vccnz .LBB0_1582
	global_load_dword v142, v[128:129], off nt
	global_load_dword v143, v[128:129], off offset:256 nt
	global_load_dword v147, v[130:131], off nt
	s_or_b32 s0, s3, s33
	s_lshl_b32 s0, s0, 22
	v_lshl_add_u64 v[136:137], v[124:125], 0, s[0:1]
	s_add_i32 s0, s33, s3
	s_lshl_b64 s[28:29], s[0:1], 9
	v_lshl_add_u64 v[138:139], v[134:135], 0, s[28:29]
	s_mov_b64 s[28:29], s[20:21]
	s_mov_b32 s30, s4
	s_branch .LBB0_1586
.LBB0_1585:
	ds_read2_b32 v[10:11], v145 offset1:4
	global_load_dwordx2 v[140:141], v[138:139], off nt
	ds_read2_b32 v[12:13], v145 offset0:8 offset1:12
	ds_read_b128 v[86:89], v144 offset:512
	ds_read_b128 v[14:17], v144 offset:528
	ds_read_b128 v[6:9], v144 offset:544
	ds_read_b128 v[2:5], v144 offset:560
	s_waitcnt lgkmcnt(3)
	v_bfe_u32 v86, v86, v146, 8
	v_ashrrev_i32_e32 v19, 31, v10
	v_mov_b32_e32 v18, v10
	v_lshlrev_b64 v[18:19], 8, v[18:19]
	v_ashrrev_i32_e32 v21, 31, v11
	v_mov_b32_e32 v20, v11
	v_lshl_add_u64 v[18:19], v[136:137], 0, v[18:19]
	v_lshlrev_b64 v[10:11], 8, v[20:21]
	v_lshl_add_u64 v[10:11], v[136:137], 0, v[10:11]
	global_load_dwordx4 v[118:121], v[18:19], off
	global_load_dwordx4 v[106:109], v[10:11], off
	v_ashrrev_i32_e32 v11, 31, v12
	v_mov_b32_e32 v10, v12
	v_lshlrev_b64 v[10:11], 8, v[10:11]
	v_ashrrev_i32_e32 v19, 31, v13
	v_mov_b32_e32 v18, v13
	v_lshl_add_u64 v[10:11], v[136:137], 0, v[10:11]
	v_lshlrev_b64 v[18:19], 8, v[18:19]
	ds_read2_b32 v[12:13], v145 offset0:16 offset1:20
	v_lshl_add_u64 v[18:19], v[136:137], 0, v[18:19]
	global_load_dwordx4 v[114:117], v[10:11], off
	global_load_dwordx4 v[98:101], v[18:19], off
	v_lshlrev_b32_e32 v86, v1, v86
	v_cndmask_b32_e64 v150, 0, v86, s[12:13]
	s_waitcnt lgkmcnt(0)
	v_ashrrev_i32_e32 v11, 31, v12
	v_mov_b32_e32 v10, v12
	v_lshlrev_b64 v[10:11], 8, v[10:11]
	v_ashrrev_i32_e32 v19, 31, v13
	v_mov_b32_e32 v18, v13
	v_lshl_add_u64 v[10:11], v[136:137], 0, v[10:11]
	v_lshlrev_b64 v[18:19], 8, v[18:19]
	ds_read2_b32 v[12:13], v145 offset0:24 offset1:28
	v_lshl_add_u64 v[18:19], v[136:137], 0, v[18:19]
	global_load_dwordx4 v[110:113], v[10:11], off
	global_load_dwordx4 v[90:93], v[18:19], off
	v_cndmask_b32_e64 v151, 0, v86, s[14:15]
	v_bfe_u32 v14, v14, v146, 8
	s_waitcnt lgkmcnt(0)
	v_ashrrev_i32_e32 v11, 31, v12
	v_mov_b32_e32 v10, v12
	v_lshlrev_b64 v[10:11], 8, v[10:11]
	v_ashrrev_i32_e32 v19, 31, v13
	v_mov_b32_e32 v18, v13
	v_lshl_add_u64 v[10:11], v[136:137], 0, v[10:11]
	v_lshlrev_b64 v[18:19], 8, v[18:19]
	ds_read2_b32 v[12:13], v145 offset0:32 offset1:36
	v_lshl_add_u64 v[18:19], v[136:137], 0, v[18:19]
	global_load_dwordx4 v[102:105], v[10:11], off
	global_load_dwordx4 v[82:85], v[18:19], off
	v_lshlrev_b32_e32 v14, v1, v14
	v_bfe_u32 v6, v6, v146, 8
	s_waitcnt lgkmcnt(0)
	v_ashrrev_i32_e32 v11, 31, v12
	v_mov_b32_e32 v10, v12
	v_lshlrev_b64 v[10:11], 8, v[10:11]
	v_ashrrev_i32_e32 v19, 31, v13
	v_mov_b32_e32 v18, v13
	v_lshl_add_u64 v[10:11], v[136:137], 0, v[10:11]
	v_lshlrev_b64 v[18:19], 8, v[18:19]
	ds_read2_b32 v[12:13], v145 offset0:40 offset1:44
	v_lshl_add_u64 v[18:19], v[136:137], 0, v[18:19]
	global_load_dwordx4 v[94:97], v[10:11], off
	global_load_dwordx4 v[74:77], v[18:19], off
	v_lshlrev_b32_e32 v6, v1, v6
	v_bfe_u32 v2, v2, v146, 8
	s_waitcnt lgkmcnt(0)
	v_ashrrev_i32_e32 v11, 31, v12
	v_mov_b32_e32 v10, v12
	v_lshlrev_b64 v[10:11], 8, v[10:11]
	v_ashrrev_i32_e32 v19, 31, v13
	v_mov_b32_e32 v18, v13
	v_lshl_add_u64 v[10:11], v[136:137], 0, v[10:11]
	ds_read2_b32 v[12:13], v145 offset0:48 offset1:52
	v_lshlrev_b64 v[18:19], 8, v[18:19]
	v_lshl_add_u64 v[18:19], v[136:137], 0, v[18:19]
	global_load_dwordx4 v[78:81], v[10:11], off
	global_load_dwordx4 v[66:69], v[18:19], off
	v_lshlrev_b32_e32 v2, v1, v2
	s_waitcnt lgkmcnt(0)
	v_ashrrev_i32_e32 v11, 31, v12
	v_mov_b32_e32 v10, v12
	v_ashrrev_i32_e32 v19, 31, v13
	v_mov_b32_e32 v18, v13
	ds_read2_b32 v[12:13], v145 offset0:56 offset1:60
	v_lshlrev_b64 v[10:11], 8, v[10:11]
	v_lshlrev_b64 v[18:19], 8, v[18:19]
	v_lshl_add_u64 v[10:11], v[136:137], 0, v[10:11]
	v_lshl_add_u64 v[18:19], v[136:137], 0, v[18:19]
	global_load_dwordx4 v[70:73], v[10:11], off
	global_load_dwordx4 v[58:61], v[18:19], off
	s_waitcnt lgkmcnt(0)
	v_ashrrev_i32_e32 v11, 31, v12
	v_mov_b32_e32 v10, v12
	v_ashrrev_i32_e32 v19, 31, v13
	v_mov_b32_e32 v18, v13
	ds_read2_b32 v[12:13], v145 offset0:64 offset1:68
	v_lshlrev_b64 v[10:11], 8, v[10:11]
	v_lshl_add_u64 v[10:11], v[136:137], 0, v[10:11]
	v_lshlrev_b64 v[18:19], 8, v[18:19]
	v_lshl_add_u64 v[18:19], v[136:137], 0, v[18:19]
	global_load_dwordx4 v[62:65], v[10:11], off
	global_load_dwordx4 v[46:49], v[18:19], off
	s_waitcnt lgkmcnt(0)
	v_ashrrev_i32_e32 v11, 31, v12
	v_mov_b32_e32 v10, v12
	v_lshlrev_b64 v[10:11], 8, v[10:11]
	v_ashrrev_i32_e32 v19, 31, v13
	v_mov_b32_e32 v18, v13
	v_lshl_add_u64 v[10:11], v[136:137], 0, v[10:11]
	ds_read2_b32 v[12:13], v145 offset0:72 offset1:76
	v_lshlrev_b64 v[18:19], 8, v[18:19]
	v_lshl_add_u64 v[18:19], v[136:137], 0, v[18:19]
	global_load_dwordx4 v[50:53], v[10:11], off
	global_load_dwordx4 v[38:41], v[18:19], off
	ds_read2_b32 v[20:21], v145 offset0:80 offset1:84
	s_waitcnt lgkmcnt(1)
	v_ashrrev_i32_e32 v19, 31, v13
	v_mov_b32_e32 v18, v13
	v_ashrrev_i32_e32 v11, 31, v12
	v_mov_b32_e32 v10, v12
	v_lshlrev_b64 v[12:13], 8, v[18:19]
	s_waitcnt lgkmcnt(0)
; __device__ __forceinline__ void phase_peer_v(const Frame& F, const Args& a, const bool dry) {
;     ...
;             for (int q8 = 0; q8 < 32 / PS_B; ++q8) { u32x4 w[PS_B]; unsigned cd[PS_B];
; #pragma unroll
;                 for (int j = 0; j < PS_B; ++j) { const int q = q8 * PS_B + j; const int e = lpe[4 * q + rg]; cd[j] = lcq[q]; w[j] = *(const u32x4*)(Vs + (size_t)e * 256); }
; #pragma unroll
;                 for (int j = 0; j < PS_B; ++j) { const unsigned cb = ((cd[j] >> (8 * rg)) & 255u) << bsh;
;                     const u32x4 av = {dsel == 0 ? cb : 0u, dsel == 1 ? cb : 0u, dsel == 2 ? cb : 0u, dsel == 3 ? cb : 0u};
;                     acc = __builtin_amdgcn_mfma_i32_16x16x64_i8(__builtin_bit_cast(i32x4, av), __builtin_bit_cast(i32x4, w[j]), acc, 0, 0, 0); } }
	v_ashrrev_i32_e32 v19, 31, v20
	v_mov_b32_e32 v18, v20
	v_ashrrev_i32_e32 v23, 31, v21
	v_mov_b32_e32 v22, v21
	v_lshlrev_b64 v[10:11], 8, v[10:11]
	v_lshlrev_b64 v[18:19], 8, v[18:19]
	v_lshlrev_b64 v[22:23], 8, v[22:23]
	v_lshl_add_u64 v[10:11], v[136:137], 0, v[10:11]
	v_lshl_add_u64 v[12:13], v[136:137], 0, v[12:13]
	v_lshl_add_u64 v[18:19], v[136:137], 0, v[18:19]
	v_lshl_add_u64 v[22:23], v[136:137], 0, v[22:23]
	global_load_dwordx4 v[42:45], v[10:11], off
	global_load_dwordx4 v[30:33], v[12:13], off
	ds_read_b128 v[54:57], v144 offset:576
	ds_read_b128 v[10:13], v144 offset:592
	ds_read2_b32 v[20:21], v145 offset0:88 offset1:92
	global_load_dwordx4 v[34:37], v[18:19], off
	s_nop 0
	global_load_dwordx4 v[22:25], v[22:23], off
	ds_read2_b32 v[152:153], v145 offset0:96 offset1:100
	s_waitcnt lgkmcnt(2)
	v_bfe_u32 v10, v10, v146, 8
	s_waitcnt lgkmcnt(1)
	v_ashrrev_i32_e32 v19, 31, v20
	v_mov_b32_e32 v18, v20
	s_waitcnt lgkmcnt(0)
	v_ashrrev_i32_e32 v149, 31, v152
	v_mov_b32_e32 v148, v152
	v_lshlrev_b64 v[148:149], 8, v[148:149]
	v_lshl_add_u64 v[156:157], v[136:137], 0, v[148:149]
	v_cndmask_b32_e64 v148, 0, v86, s[8:9]
	v_cndmask_b32_e64 v149, 0, v86, s[10:11]
	v_bfe_u32 v86, v87, v146, 8
	v_lshlrev_b32_e32 v86, v1, v86
	s_waitcnt vmcnt(21)
	v_mfma_i32_16x16x64_i8 v[118:121], v[148:151], v[118:121], 0
	v_cndmask_b32_e64 v148, 0, v86, s[8:9]
	v_cndmask_b32_e64 v149, 0, v86, s[10:11]
	v_cndmask_b32_e64 v150, 0, v86, s[12:13]
	v_cndmask_b32_e64 v151, 0, v86, s[14:15]
	v_ashrrev_i32_e32 v155, 31, v153
	v_mov_b32_e32 v154, v153
	v_bfe_u32 v86, v88, v146, 8
	v_lshlrev_b64 v[152:153], 8, v[154:155]
	v_lshlrev_b32_e32 v86, v1, v86
	v_lshl_add_u64 v[158:159], v[136:137], 0, v[152:153]
	v_cndmask_b32_e64 v152, 0, v86, s[8:9]
	v_cndmask_b32_e64 v153, 0, v86, s[10:11]
	v_cndmask_b32_e64 v154, 0, v86, s[12:13]
	v_cndmask_b32_e64 v155, 0, v86, s[14:15]
	s_waitcnt vmcnt(20)
	v_mfma_i32_16x16x64_i8 v[148:151], v[148:151], v[106:109], v[118:121]
	v_bfe_u32 v86, v89, v146, 8
	v_ashrrev_i32_e32 v27, 31, v21
	v_mov_b32_e32 v26, v21
	v_lshlrev_b32_e32 v89, v1, v86
	v_lshlrev_b64 v[18:19], 8, v[18:19]
	v_lshlrev_b64 v[20:21], 8, v[26:27]
	v_cndmask_b32_e64 v86, 0, v89, s[8:9]
	v_cndmask_b32_e64 v87, 0, v89, s[10:11]
	v_cndmask_b32_e64 v88, 0, v89, s[12:13]
	v_cndmask_b32_e64 v89, 0, v89, s[14:15]
	v_lshl_add_u64 v[18:19], v[136:137], 0, v[18:19]
	v_lshl_add_u64 v[20:21], v[136:137], 0, v[20:21]
	s_waitcnt vmcnt(19)
	v_mfma_i32_16x16x64_i8 v[114:117], v[152:155], v[114:117], v[148:151]
	global_load_dwordx4 v[26:29], v[18:19], off
	s_nop 0
	global_load_dwordx4 v[18:21], v[20:21], off
	s_nop 0
	global_load_dwordx4 v[118:121], v[156:157], off
	global_load_dwordx4 v[106:109], v[158:159], off
	ds_read2_b32 v[156:157], v145 offset0:104 offset1:108
	v_cndmask_b32_e64 v148, 0, v14, s[8:9]
	v_cndmask_b32_e64 v149, 0, v14, s[10:11]
	v_cndmask_b32_e64 v150, 0, v14, s[12:13]
	v_cndmask_b32_e64 v151, 0, v14, s[14:15]
	s_waitcnt vmcnt(22)
	v_mfma_i32_16x16x64_i8 v[86:89], v[86:89], v[98:101], v[114:117]
	v_bfe_u32 v14, v15, v146, 8
	s_waitcnt lgkmcnt(0)
	v_ashrrev_i32_e32 v99, 31, v156
	v_mov_b32_e32 v98, v156
	v_lshlrev_b32_e32 v14, v1, v14
	v_lshlrev_b64 v[114:115], 8, v[98:99]
	v_cndmask_b32_e64 v98, 0, v14, s[8:9]
	v_cndmask_b32_e64 v99, 0, v14, s[10:11]
	v_cndmask_b32_e64 v100, 0, v14, s[12:13]
	v_cndmask_b32_e64 v101, 0, v14, s[14:15]
	s_waitcnt vmcnt(21)
	v_mfma_i32_16x16x64_i8 v[86:89], v[148:151], v[110:113], v[86:89]
	v_bfe_u32 v14, v16, v146, 8
	v_lshlrev_b32_e32 v14, v1, v14
	v_cndmask_b32_e64 v110, 0, v14, s[8:9]
	v_cndmask_b32_e64 v111, 0, v14, s[10:11]
	v_cndmask_b32_e64 v112, 0, v14, s[12:13]
	v_cndmask_b32_e64 v113, 0, v14, s[14:15]
	s_waitcnt vmcnt(20)
	v_mfma_i32_16x16x64_i8 v[86:89], v[98:101], v[90:93], v[86:89]
	v_bfe_u32 v14, v17, v146, 8
	v_lshlrev_b32_e32 v17, v1, v14
	v_cndmask_b32_e64 v14, 0, v17, s[8:9]
	v_cndmask_b32_e64 v15, 0, v17, s[10:11]
	v_cndmask_b32_e64 v16, 0, v17, s[12:13]
	v_cndmask_b32_e64 v17, 0, v17, s[14:15]
	s_waitcnt vmcnt(19)
	v_mfma_i32_16x16x64_i8 v[86:89], v[110:113], v[102:105], v[86:89]
	v_cndmask_b32_e64 v90, 0, v6, s[8:9]
	v_cndmask_b32_e64 v91, 0, v6, s[10:11]
	v_cndmask_b32_e64 v92, 0, v6, s[12:13]
	v_cndmask_b32_e64 v93, 0, v6, s[14:15]
	s_waitcnt vmcnt(18)
	v_mfma_i32_16x16x64_i8 v[14:17], v[14:17], v[82:85], v[86:89]
	v_ashrrev_i32_e32 v101, 31, v157
	v_mov_b32_e32 v100, v157
	v_bfe_u32 v6, v7, v146, 8
	v_lshlrev_b64 v[82:83], 8, v[100:101]
	v_lshlrev_b32_e32 v6, v1, v6
	v_lshl_add_u64 v[100:101], v[136:137], 0, v[82:83]
	v_cndmask_b32_e64 v82, 0, v6, s[8:9]
	v_cndmask_b32_e64 v83, 0, v6, s[10:11]
	v_cndmask_b32_e64 v84, 0, v6, s[12:13]
	v_cndmask_b32_e64 v85, 0, v6, s[14:15]
	s_waitcnt vmcnt(17)
	v_mfma_i32_16x16x64_i8 v[14:17], v[90:93], v[94:97], v[14:17]
	v_bfe_u32 v6, v8, v146, 8
	v_lshlrev_b32_e32 v6, v1, v6
	ds_read2_b32 v[102:103], v145 offset0:112 offset1:116
	s_waitcnt vmcnt(16)
	v_mfma_i32_16x16x64_i8 v[14:17], v[82:85], v[74:77], v[14:17]
	v_cndmask_b32_e64 v74, 0, v6, s[8:9]
	v_cndmask_b32_e64 v75, 0, v6, s[10:11]
	v_cndmask_b32_e64 v76, 0, v6, s[12:13]
	v_cndmask_b32_e64 v77, 0, v6, s[14:15]
	v_bfe_u32 v6, v9, v146, 8
	v_lshlrev_b32_e32 v9, v1, v6
	v_cndmask_b32_e64 v6, 0, v9, s[8:9]
	v_cndmask_b32_e64 v7, 0, v9, s[10:11]
	v_cndmask_b32_e64 v8, 0, v9, s[12:13]
	v_cndmask_b32_e64 v9, 0, v9, s[14:15]
	s_waitcnt vmcnt(15)
	v_mfma_i32_16x16x64_i8 v[14:17], v[74:77], v[78:81], v[14:17]
	v_lshl_add_u64 v[98:99], v[136:137], 0, v[114:115]
	global_load_dwordx4 v[86:89], v[98:99], off
	global_load_dwordx4 v[90:93], v[100:101], off
	ds_read_b128 v[74:77], v144 offset:608
	ds_read_b128 v[78:81], v144 offset:624
	s_waitcnt vmcnt(16)
; __device__ __forceinline__ void phase_peer_v(const Frame& F, const Args& a, const bool dry) {
;     ...
;             for (int q8 = 0; q8 < 32 / PS_B; ++q8) { u32x4 w[PS_B]; unsigned cd[PS_B];
; #pragma unroll
;                 for (int j = 0; j < PS_B; ++j) { const int q = q8 * PS_B + j; const int e = lpe[4 * q + rg]; cd[j] = lcq[q]; w[j] = *(const u32x4*)(Vs + (size_t)e * 256); }
; #pragma unroll
;                 for (int j = 0; j < PS_B; ++j) { const unsigned cb = ((cd[j] >> (8 * rg)) & 255u) << bsh;
;                     const u32x4 av = {dsel == 0 ? cb : 0u, dsel == 1 ? cb : 0u, dsel == 2 ? cb : 0u, dsel == 3 ? cb : 0u};
;                     acc = __builtin_amdgcn_mfma_i32_16x16x64_i8(__builtin_bit_cast(i32x4, av), __builtin_bit_cast(i32x4, w[j]), acc, 0, 0, 0); } }
	v_mfma_i32_16x16x64_i8 v[6:9], v[6:9], v[66:69], v[14:17]
	s_waitcnt lgkmcnt(2)
	v_ashrrev_i32_e32 v95, 31, v102
	v_mov_b32_e32 v94, v102
	v_lshlrev_b64 v[82:83], 8, v[94:95]
	v_cndmask_b32_e64 v14, 0, v2, s[8:9]
	v_cndmask_b32_e64 v15, 0, v2, s[10:11]
	v_cndmask_b32_e64 v16, 0, v2, s[12:13]
	v_cndmask_b32_e64 v17, 0, v2, s[14:15]
	v_bfe_u32 v2, v3, v146, 8
	v_lshlrev_b32_e32 v2, v1, v2
	v_cndmask_b32_e64 v66, 0, v2, s[8:9]
	v_cndmask_b32_e64 v67, 0, v2, s[10:11]
	v_cndmask_b32_e64 v68, 0, v2, s[12:13]
	v_cndmask_b32_e64 v69, 0, v2, s[14:15]
	s_waitcnt vmcnt(15)
	v_mfma_i32_16x16x64_i8 v[6:9], v[14:17], v[70:73], v[6:9]
	v_bfe_u32 v2, v4, v146, 8
	v_lshlrev_b32_e32 v2, v1, v2
	v_cndmask_b32_e64 v14, 0, v2, s[8:9]
	v_cndmask_b32_e64 v15, 0, v2, s[10:11]
	v_cndmask_b32_e64 v16, 0, v2, s[12:13]
	v_cndmask_b32_e64 v17, 0, v2, s[14:15]
	s_waitcnt vmcnt(14)
	v_mfma_i32_16x16x64_i8 v[6:9], v[66:69], v[58:61], v[6:9]
	v_bfe_u32 v2, v5, v146, 8
	v_lshlrev_b32_e32 v5, v1, v2
	v_cndmask_b32_e64 v2, 0, v5, s[8:9]
	v_cndmask_b32_e64 v3, 0, v5, s[10:11]
	v_cndmask_b32_e64 v4, 0, v5, s[12:13]
	v_cndmask_b32_e64 v5, 0, v5, s[14:15]
	s_waitcnt vmcnt(13)
	v_mfma_i32_16x16x64_i8 v[6:9], v[14:17], v[62:65], v[6:9]
	v_ashrrev_i32_e32 v73, 31, v103
	v_mov_b32_e32 v72, v103
	v_lshlrev_b64 v[14:15], 8, v[72:73]
	s_waitcnt vmcnt(12)
	v_mfma_i32_16x16x64_i8 v[2:5], v[2:5], v[46:49], v[6:9]
	v_lshl_add_u64 v[58:59], v[136:137], 0, v[14:15]
	v_bfe_u32 v14, v55, v146, 8
	v_lshlrev_b32_e32 v17, v1, v14
	v_bfe_u32 v6, v54, v146, 8
	v_lshlrev_b32_e32 v9, v1, v6
	v_cndmask_b32_e64 v6, 0, v9, s[8:9]
	v_cndmask_b32_e64 v7, 0, v9, s[10:11]
	v_cndmask_b32_e64 v8, 0, v9, s[12:13]
	v_cndmask_b32_e64 v9, 0, v9, s[14:15]
	v_cndmask_b32_e64 v14, 0, v17, s[8:9]
	v_cndmask_b32_e64 v15, 0, v17, s[10:11]
	v_cndmask_b32_e64 v16, 0, v17, s[12:13]
	v_cndmask_b32_e64 v17, 0, v17, s[14:15]
	s_waitcnt vmcnt(11)
	v_mfma_i32_16x16x64_i8 v[2:5], v[6:9], v[50:53], v[2:5]
	ds_read2_b32 v[60:61], v145 offset0:120 offset1:124
	v_lshl_add_u64 v[70:71], v[136:137], 0, v[82:83]
	global_load_dwordx4 v[6:9], v[70:71], off
	global_load_dwordx4 v[46:49], v[58:59], off
	s_waitcnt vmcnt(12)
	v_mfma_i32_16x16x64_i8 v[2:5], v[14:17], v[38:41], v[2:5]
	v_bfe_u32 v14, v56, v146, 8
	v_lshlrev_b32_e32 v17, v1, v14
	v_cndmask_b32_e64 v14, 0, v17, s[8:9]
	v_cndmask_b32_e64 v15, 0, v17, s[10:11]
	v_cndmask_b32_e64 v16, 0, v17, s[12:13]
	v_cndmask_b32_e64 v17, 0, v17, s[14:15]
	v_bfe_u32 v38, v57, v146, 8
	v_lshlrev_b32_e32 v41, v1, v38
	v_cndmask_b32_e64 v38, 0, v41, s[8:9]
	v_cndmask_b32_e64 v39, 0, v41, s[10:11]
	v_cndmask_b32_e64 v40, 0, v41, s[12:13]
	v_cndmask_b32_e64 v41, 0, v41, s[14:15]
	s_waitcnt vmcnt(11)
	v_mfma_i32_16x16x64_i8 v[2:5], v[14:17], v[42:45], v[2:5]
	s_waitcnt lgkmcnt(0)
	v_ashrrev_i32_e32 v51, 31, v60
	v_mov_b32_e32 v50, v60
	v_lshlrev_b64 v[14:15], 8, v[50:51]
	v_lshlrev_b32_e32 v10, v1, v10
	v_lshl_add_u64 v[42:43], v[136:137], 0, v[14:15]
	v_cndmask_b32_e64 v14, 0, v10, s[8:9]
	v_cndmask_b32_e64 v15, 0, v10, s[10:11]
	v_cndmask_b32_e64 v16, 0, v10, s[12:13]
	v_cndmask_b32_e64 v17, 0, v10, s[14:15]
	s_waitcnt vmcnt(10)
	v_mfma_i32_16x16x64_i8 v[2:5], v[38:41], v[30:33], v[2:5]
	v_bfe_u32 v10, v11, v146, 8
	v_lshlrev_b32_e32 v10, v1, v10
	v_cndmask_b32_e64 v30, 0, v10, s[8:9]
	v_cndmask_b32_e64 v31, 0, v10, s[10:11]
	v_cndmask_b32_e64 v32, 0, v10, s[12:13]
	v_cndmask_b32_e64 v33, 0, v10, s[14:15]
	s_waitcnt vmcnt(9)
	v_mfma_i32_16x16x64_i8 v[2:5], v[14:17], v[34:37], v[2:5]
	v_ashrrev_i32_e32 v11, 31, v61
	v_mov_b32_e32 v10, v61
	v_lshlrev_b64 v[34:35], 8, v[10:11]
	v_bfe_u32 v10, v12, v146, 8
	v_lshlrev_b32_e32 v10, v1, v10
	v_cndmask_b32_e64 v14, 0, v10, s[8:9]
	v_cndmask_b32_e64 v15, 0, v10, s[10:11]
	v_cndmask_b32_e64 v16, 0, v10, s[12:13]
	v_cndmask_b32_e64 v17, 0, v10, s[14:15]
	s_waitcnt vmcnt(8)
; __device__ __forceinline__ unsigned cvtpk(float lo, float hi) { unsigned r; asm volatile("v_cvt_pk_bf16_f32 %0, %1, %2" : "=v"(r) : "v"(lo), "v"(hi)); return r; }
; __device__ __forceinline__ void phase_peer_v(const Frame& F, const Args& a, const bool dry) {
;     ...
;             u32x2* xp = (u32x2*)(X + (size_t)tok * D + sl * 256 + li * 16 + rg * 4);
;             const u32x2 xb = *xp; const f32x4 xq = {bflo(xb.x), bfhi(xb.x), bflo(xb.y), bfhi(xb.y)};
;             const float csc = CSC[tok];
;             i32x4 acc = {0, 0, 0, 0};
; #pragma unroll
;             for (int q8 = 0; q8 < 32 / PS_B; ++q8) { u32x4 w[PS_B]; unsigned cd[PS_B];
; #pragma unroll
;                 for (int j = 0; j < PS_B; ++j) { const int q = q8 * PS_B + j; const int e = lpe[4 * q + rg]; cd[j] = lcq[q]; w[j] = *(const u32x4*)(Vs + (size_t)e * 256); }
; #pragma unroll
;                 for (int j = 0; j < PS_B; ++j) { const unsigned cb = ((cd[j] >> (8 * rg)) & 255u) << bsh;
;                     const u32x4 av = {dsel == 0 ? cb : 0u, dsel == 1 ? cb : 0u, dsel == 2 ? cb : 0u, dsel == 3 ? cb : 0u};
;                     acc = __builtin_amdgcn_mfma_i32_16x16x64_i8(__builtin_bit_cast(i32x4, av), __builtin_bit_cast(i32x4, w[j]), acc, 0, 0, 0); } }
;             if (!dry) { f32x4 x0 = xq; x0.x += (float)acc[0] * csc; x0.y += (float)acc[1] * csc; x0.z += (float)acc[2] * csc; x0.w += (float)acc[3] * csc; *xp = (u32x2){cvtpk(x0.x, x0.y), cvtpk(x0.z, x0.w)}; }
	v_mfma_i32_16x16x64_i8 v[2:5], v[30:33], v[22:25], v[2:5]
	v_lshl_add_u64 v[22:23], v[136:137], 0, v[34:35]
	v_bfe_u32 v10, v13, v146, 8
	v_lshlrev_b32_e32 v13, v1, v10
	s_waitcnt vmcnt(7)
	v_mfma_i32_16x16x64_i8 v[2:5], v[14:17], v[26:29], v[2:5]
	global_load_dwordx4 v[14:17], v[42:43], off
	s_nop 0
	global_load_dwordx4 v[22:25], v[22:23], off
	v_cndmask_b32_e64 v10, 0, v13, s[8:9]
	v_cndmask_b32_e64 v11, 0, v13, s[10:11]
	v_cndmask_b32_e64 v12, 0, v13, s[12:13]
	v_cndmask_b32_e64 v13, 0, v13, s[14:15]
	s_waitcnt vmcnt(8)
	s_nop 0
	v_mfma_i32_16x16x64_i8 v[2:5], v[10:13], v[18:21], v[2:5]
	global_load_dword v18, v123, s[28:29] nt
	v_bfe_u32 v10, v74, v146, 8
	v_lshlrev_b32_e32 v13, v1, v10
	v_cndmask_b32_e64 v10, 0, v13, s[8:9]
	v_cndmask_b32_e64 v11, 0, v13, s[10:11]
	v_cndmask_b32_e64 v12, 0, v13, s[12:13]
	v_cndmask_b32_e64 v13, 0, v13, s[14:15]
	v_lshlrev_b32_e32 v19, 16, v140
	s_add_u32 s28, s28, s22
	s_waitcnt vmcnt(8)
	v_mfma_i32_16x16x64_i8 v[2:5], v[10:13], v[118:121], v[2:5]
	v_bfe_u32 v10, v75, v146, 8
	v_lshlrev_b32_e32 v13, v1, v10
	v_cndmask_b32_e64 v10, 0, v13, s[8:9]
	v_cndmask_b32_e64 v11, 0, v13, s[10:11]
	v_cndmask_b32_e64 v12, 0, v13, s[12:13]
	v_cndmask_b32_e64 v13, 0, v13, s[14:15]
	s_addc_u32 s29, s29, s23
	s_andn2_b64 vcc, exec, s[34:35]
	s_waitcnt vmcnt(7)
	v_mfma_i32_16x16x64_i8 v[2:5], v[10:13], v[106:109], v[2:5]
	v_bfe_u32 v10, v76, v146, 8
	v_lshlrev_b32_e32 v13, v1, v10
	v_cndmask_b32_e64 v10, 0, v13, s[8:9]
	v_cndmask_b32_e64 v11, 0, v13, s[10:11]
	v_cndmask_b32_e64 v12, 0, v13, s[12:13]
	v_cndmask_b32_e64 v13, 0, v13, s[14:15]
	s_waitcnt vmcnt(6)
	s_nop 0
	v_mfma_i32_16x16x64_i8 v[2:5], v[10:13], v[86:89], v[2:5]
	v_bfe_u32 v10, v77, v146, 8
	v_lshlrev_b32_e32 v13, v1, v10
	v_cndmask_b32_e64 v10, 0, v13, s[8:9]
	v_cndmask_b32_e64 v11, 0, v13, s[10:11]
	v_cndmask_b32_e64 v12, 0, v13, s[12:13]
	v_cndmask_b32_e64 v13, 0, v13, s[14:15]
	s_waitcnt vmcnt(5)
	s_nop 0
	v_mfma_i32_16x16x64_i8 v[2:5], v[10:13], v[90:93], v[2:5]
	v_bfe_u32 v10, v78, v146, 8
	v_lshlrev_b32_e32 v13, v1, v10
	v_cndmask_b32_e64 v10, 0, v13, s[8:9]
	v_cndmask_b32_e64 v11, 0, v13, s[10:11]
	v_cndmask_b32_e64 v12, 0, v13, s[12:13]
	v_cndmask_b32_e64 v13, 0, v13, s[14:15]
	s_waitcnt vmcnt(4)
	s_nop 0
	v_mfma_i32_16x16x64_i8 v[2:5], v[10:13], v[6:9], v[2:5]
	v_bfe_u32 v6, v79, v146, 8
	v_lshlrev_b32_e32 v9, v1, v6
	v_cndmask_b32_e64 v6, 0, v9, s[8:9]
	v_cndmask_b32_e64 v7, 0, v9, s[10:11]
	v_cndmask_b32_e64 v8, 0, v9, s[12:13]
	v_cndmask_b32_e64 v9, 0, v9, s[14:15]
	v_bfe_u32 v10, v81, v146, 8
	v_lshlrev_b32_e32 v13, v1, v10
	s_waitcnt vmcnt(3)
	v_mfma_i32_16x16x64_i8 v[2:5], v[6:9], v[46:49], v[2:5]
	v_bfe_u32 v6, v80, v146, 8
	v_lshlrev_b32_e32 v9, v1, v6
	v_cndmask_b32_e64 v6, 0, v9, s[8:9]
	v_cndmask_b32_e64 v7, 0, v9, s[10:11]
	v_cndmask_b32_e64 v8, 0, v9, s[12:13]
	v_cndmask_b32_e64 v9, 0, v9, s[14:15]
	v_cndmask_b32_e64 v10, 0, v13, s[8:9]
	v_cndmask_b32_e64 v11, 0, v13, s[10:11]
	v_cndmask_b32_e64 v12, 0, v13, s[12:13]
	v_cndmask_b32_e64 v13, 0, v13, s[14:15]
	s_waitcnt vmcnt(2)
	v_mfma_i32_16x16x64_i8 v[2:5], v[6:9], v[14:17], v[2:5]
	v_and_b32_e32 v6, 0xffff0000, v140
	v_lshlrev_b32_e32 v7, 16, v141
	v_and_b32_e32 v8, 0xffff0000, v141
	s_waitcnt vmcnt(1)
	v_mfma_i32_16x16x64_i8 v[2:5], v[10:13], v[22:25], v[2:5]
	s_nop 7
	v_cvt_f32_i32_e32 v2, v2
	v_cvt_f32_i32_e32 v3, v3
	v_cvt_f32_i32_e32 v4, v4
	v_cvt_f32_i32_e32 v5, v5
	s_waitcnt vmcnt(0)
	v_fmac_f32_e32 v19, v18, v2
	v_fmac_f32_e32 v6, v18, v3
	v_fmac_f32_e32 v7, v18, v4
	v_fmac_f32_e32 v8, v18, v5
	v_cvt_pk_bf16_f32 v2, v19, v6
	v_cvt_pk_bf16_f32 v3, v7, v8
	global_store_dwordx2 v[138:139], v[2:3], off nt
	s_waitcnt lgkmcnt(0)
	v_lshl_add_u64 v[138:139], v[138:139], 0, s[24:25]
	s_cbranch_vccz .LBB0_1582

; #define LDS_WAIT() asm volatile("s_waitcnt lgkmcnt(0)" ::: "memory")
; __device__ __forceinline__ void phase_peer_v(const Frame& F, const Args& a, const bool dry) {
;     ...
;         for (; tok < T; tok += nrank * 8) {
;             lpe[lane] = pn0; lpe[64 + lane] = pn1; if (lane < 32) lcq[lane] = cn;
;             LDS_WAIT();
;             { const int tn = tok + nrank * 8; if (tn < T) { pn0 = PE[(size_t)tn * 128 + lane]; pn1 = PE[(size_t)tn * 128 + 64 + lane]; cn = CQ[(size_t)tn * 32 + (lane & 31)]; } }
.LBB0_1588:
	s_or_b64 exec, exec, s[34:35]
	s_add_i32 s30, s30, s2
	s_waitcnt lgkmcnt(0)
	s_cmpk_gt_i32 s30, 0x1fff
	s_cselect_b64 s[34:35], -1, 0
	s_and_b64 vcc, exec, s[34:35]
	s_cbranch_vccnz .LBB0_1585
	s_ashr_i32 s31, s30, 31
	s_lshl_b64 s[36:37], s[30:31], 7
	v_lshl_add_u64 v[2:3], v[126:127], 0, s[36:37]
	s_lshl_b64 s[36:37], s[30:31], 9
	v_lshl_add_u64 v[4:5], v[132:133], 0, s[36:37]
	global_load_dword v142, v[4:5], off nt
	global_load_dword v143, v[4:5], off offset:256 nt
	global_load_dword v147, v[2:3], off nt
	s_branch .LBB0_1585
